# attention tile loop: K reads issued before score init, score chains finish in place (no post-QK register shuffle)
# speedup vs baseline: 1.0092x; 1.0055x over previous
.LBB0_397:
	s_add_i32 s0, s34, 0x80
	s_cmp_le_u32 s0, s24
	s_cselect_b64 s[78:79], -1, 0
	s_add_i32 s82, s31, 0
	s_add_i32 s3, s34, 0x13f
	s_cmp_gt_u32 s3, s16
	s_cselect_b64 s[36:37], -1, 0
	s_cmp_gt_u32 s0, s24
	s_cbranch_scc1 .Latt_noqk
	v_add_u32_e32 v152, s82, v164
	ds_read_b128 v[204:207], v152
	ds_read_b128 v[208:211], v152 offset:512
	ds_read_b128 v[212:215], v152 offset:2048
	ds_read_b128 v[216:219], v152 offset:2560
	v_cndmask_b32_e64 v68, v165, 0, s[36:37]
	v_sub_f32_e32 v68, v68, v167
	v_mov_b32_e32 v82, v68
	v_mov_b32_e32 v83, v68
	v_mov_b32_e32 v69, v68
	v_mov_b32_e32 v70, v68
	v_mov_b32_e32 v71, v68
	v_mov_b32_e32 v72, v68
	v_mov_b32_e32 v73, v68
	v_mov_b32_e32 v74, v68
	v_mov_b32_e32 v75, v68
	v_mov_b32_e32 v76, v68
	v_mov_b32_e32 v77, v68
	v_mov_b32_e32 v78, v68
	v_mov_b32_e32 v79, v68
	v_mov_b32_e32 v80, v68
	v_mov_b32_e32 v81, v68
	s_nop 1
	s_waitcnt lgkmcnt(3)
	v_mfma_f32_32x32x16_bf16 v[100:115], v[204:207], v[116:119], v[68:83]
	s_waitcnt lgkmcnt(2)
	v_mfma_f32_32x32x16_bf16 v[84:99], v[208:211], v[116:119], v[68:83]
	s_waitcnt lgkmcnt(1)
	v_mfma_f32_32x32x16_bf16 v[100:115], v[212:215], v[120:123], v[100:115]
	ds_read_b128 v[204:207], v152 offset:4096
	ds_read_b128 v[208:211], v152 offset:4608
	ds_read_b128 v[212:215], v152 offset:6144
	ds_read_b128 v[178:181], v152 offset:6656
	s_waitcnt lgkmcnt(4)
	v_mfma_f32_32x32x16_bf16 v[84:99], v[216:219], v[120:123], v[84:99]
	s_waitcnt lgkmcnt(3)
	v_mfma_f32_32x32x16_bf16 v[100:115], v[204:207], v[124:127], v[100:115]
	s_waitcnt lgkmcnt(2)
	v_mfma_f32_32x32x16_bf16 v[84:99], v[208:211], v[124:127], v[84:99]
	s_waitcnt lgkmcnt(1)
	v_mfma_f32_32x32x16_bf16 v[68:83], v[212:215], v[128:131], v[100:115]
	s_waitcnt lgkmcnt(0)
	v_mfma_f32_32x32x16_bf16 v[84:99], v[178:181], v[128:131], v[84:99]
	s_andn2_b64 vcc, exec, s[36:37]
	s_cbranch_vccnz .LBB0_432
	v_add_u32_e32 v177, s5, v176
	s_mov_b32 s100, 0x207a4
	v_lshl_add_u32 v177, v177, 2, s100
	ds_read2_b32 v[204:205], v177 offset0:55 offset1:54
	ds_read2_b32 v[206:207], v177 offset0:53 offset1:52
	ds_read2_b32 v[208:209], v177 offset0:51 offset1:50
	ds_read2_b32 v[210:211], v177 offset0:49 offset1:48
	ds_read2_b32 v[212:213], v177 offset0:39 offset1:38
	ds_read2_b32 v[214:215], v177 offset0:37 offset1:36
	ds_read2_b32 v[216:217], v177 offset0:35 offset1:34
	ds_read2_b32 v[218:219], v177 offset0:33 offset1:32
	ds_read2_b32 v[220:221], v177 offset0:23 offset1:22
	ds_read2_b32 v[222:223], v177 offset0:21 offset1:20
	ds_read2_b32 v[224:225], v177 offset0:19 offset1:18
	ds_read2_b32 v[226:227], v177 offset0:17 offset1:16
	ds_read2_b32 v[228:229], v177 offset0:7 offset1:6
	ds_read2_b32 v[230:231], v177 offset0:5 offset1:4
	ds_read2_b32 v[232:233], v177 offset0:3 offset1:2
	s_waitcnt lgkmcnt(14)
	v_pk_add_f32 v[68:69], v[68:69], v[204:205]
	ds_read2_b32 v[204:205], v177 offset0:1 offset1:0
	s_waitcnt lgkmcnt(8)
	v_pk_add_f32 v[70:71], v[70:71], v[206:207]
	v_pk_add_f32 v[72:73], v[72:73], v[208:209]
	v_pk_add_f32 v[74:75], v[74:75], v[210:211]
	v_pk_add_f32 v[76:77], v[76:77], v[212:213]
	v_pk_add_f32 v[78:79], v[78:79], v[214:215]
	v_pk_add_f32 v[80:81], v[80:81], v[216:217]
	v_pk_add_f32 v[82:83], v[82:83], v[218:219]
	s_waitcnt lgkmcnt(0)
	v_pk_add_f32 v[84:85], v[84:85], v[220:221]
	v_pk_add_f32 v[86:87], v[86:87], v[222:223]
	v_pk_add_f32 v[88:89], v[88:89], v[224:225]
	v_pk_add_f32 v[90:91], v[90:91], v[226:227]
	v_pk_add_f32 v[92:93], v[92:93], v[228:229]
	v_pk_add_f32 v[94:95], v[94:95], v[230:231]
	v_pk_add_f32 v[96:97], v[96:97], v[232:233]
	v_pk_add_f32 v[98:99], v[98:99], v[204:205]
.LBB0_432:
	s_add_i32 s34, s34, 64
	s_cmp_gt_u32 s34, s24
	s_cbranch_scc0 .LBB0_435

.Latt_noqk:
	v_cndmask_b32_e64 v68, v165, 0, s[36:37]
	v_sub_f32_e32 v68, v68, v167
	v_mov_b32_e32 v82, v68
	v_mov_b32_e32 v83, v68
	v_mov_b32_e32 v69, v68
	v_mov_b32_e32 v70, v68
	v_mov_b32_e32 v71, v68
	v_mov_b32_e32 v72, v68
	v_mov_b32_e32 v73, v68
	v_mov_b32_e32 v74, v68
	v_mov_b32_e32 v75, v68
	v_mov_b32_e32 v76, v68
	v_mov_b32_e32 v77, v68
	v_mov_b32_e32 v78, v68
	v_mov_b32_e32 v79, v68
	v_mov_b32_e32 v80, v68
	v_mov_b32_e32 v81, v68
	v_mov_b64_e32 v[98:99], v[82:83]
	v_mov_b64_e32 v[96:97], v[80:81]
	v_mov_b64_e32 v[94:95], v[78:79]
	v_mov_b64_e32 v[92:93], v[76:77]
	v_mov_b64_e32 v[90:91], v[74:75]
	v_mov_b64_e32 v[88:89], v[72:73]
	v_mov_b64_e32 v[86:87], v[70:71]
	v_mov_b64_e32 v[84:85], v[68:69]
